# expert GEMM 1 epilogue: clamped-SwiGLU on packed f32 ops four elements at a time, in place in the accumulators (12 of 16 quads): 7 issue slots per element instead of 12
# speedup vs baseline: 1.0058x; 1.0033x over previous
.LBB0_1265:
	s_mov_b32 s84, 0xc01d265f
	v_mov_b32_e32 v8, v0
	v_ashrrev_i32_e32 v181, 31, v180
	v_ashrrev_i32_e32 v2, 2, v8
	v_and_b32_e32 v6, 0xffffffc0, v2
	v_lshlrev_b64 v[4:5], 8, v[180:181]
	v_ashrrev_i32_e32 v7, 31, v6
	v_and_or_b32 v6, v8, 15, v6
	v_bfe_u32 v12, v8, 4, 1
	v_lshl_add_u64 v[10:11], v[6:7], 0, v[4:5]
	v_lshlrev_b32_e32 v4, 3, v12
	v_lshrrev_b32_e32 v2, 1, v8
	v_sub_co_u32_e32 v8, vcc, 0, v4
	s_nop 0
	v_subb_co_u32_e64 v9, s[2:3], 0, 0, vcc
	s_mov_b32 s2, 0xc1c00000
	v_med3_f32 v172, v172, s2, v200
	v_med3_f32 v173, v173, s2, v200
	v_med3_f32 v174, v174, s2, v200
	v_med3_f32 v175, v175, s2, v200
	v_med3_f32 v164, v164, s2, v200
	v_med3_f32 v165, v165, s2, v200
	v_med3_f32 v166, v166, s2, v200
	v_med3_f32 v167, v167, s2, v200
	v_med3_f32 v150, v150, s2, v200
	v_med3_f32 v151, v151, s2, v200
	v_lshlrev_b32_e32 v12, 4, v12
	s_lshl_b32 s12, s26, 7
	s_ashr_i32 s13, s12, 31
	v_and_b32_e32 v2, 0x78, v2
	v_med3_f32 v87, v87, s2, v200
	s_and_b64 vcc, exec, s[40:41]
	v_min_f32_e32 v176, 0x40e00000, v176
	v_min_f32_e32 v177, 0x40e00000, v177
	v_min_f32_e32 v178, 0x40e00000, v178
	v_min_f32_e32 v179, 0x40e00000, v179
	v_pk_mul_f32 v[172:173], v[176:177], v[172:173]
	v_pk_mul_f32 v[174:175], v[178:179], v[174:175]
	v_pk_mul_f32 v[176:177], v[176:177], s[84:85] op_sel_hi:[1,0]
	v_pk_mul_f32 v[178:179], v[178:179], s[84:85] op_sel_hi:[1,0]
	v_exp_f32_e32 v176, v176
	v_exp_f32_e32 v177, v177
	v_exp_f32_e32 v178, v178
	v_exp_f32_e32 v179, v179
	v_pk_add_f32 v[176:177], v[176:177], 1.0 op_sel_hi:[1,0]
	v_pk_add_f32 v[178:179], v[178:179], 1.0 op_sel_hi:[1,0]
	v_rcp_f32_e32 v176, v176
	v_rcp_f32_e32 v177, v177
	v_rcp_f32_e32 v178, v178
	v_rcp_f32_e32 v179, v179
	v_pk_mul_f32 v[172:173], v[176:177], v[172:173]
	v_pk_mul_f32 v[174:175], v[178:179], v[174:175]
	v_min_f32_e32 v168, 0x40e00000, v168
	v_min_f32_e32 v169, 0x40e00000, v169
	v_min_f32_e32 v170, 0x40e00000, v170
	v_min_f32_e32 v171, 0x40e00000, v171
	v_pk_mul_f32 v[164:165], v[168:169], v[164:165]
	v_pk_mul_f32 v[166:167], v[170:171], v[166:167]
	v_pk_mul_f32 v[168:169], v[168:169], s[84:85] op_sel_hi:[1,0]
	v_pk_mul_f32 v[170:171], v[170:171], s[84:85] op_sel_hi:[1,0]
	v_exp_f32_e32 v168, v168
	v_exp_f32_e32 v169, v169
	v_exp_f32_e32 v170, v170
	v_exp_f32_e32 v171, v171
	v_pk_add_f32 v[168:169], v[168:169], 1.0 op_sel_hi:[1,0]
	v_pk_add_f32 v[170:171], v[170:171], 1.0 op_sel_hi:[1,0]
	v_rcp_f32_e32 v168, v168
	v_rcp_f32_e32 v169, v169
	v_rcp_f32_e32 v170, v170
	v_rcp_f32_e32 v171, v171
	v_pk_mul_f32 v[164:165], v[168:169], v[164:165]
	v_pk_mul_f32 v[166:167], v[170:171], v[166:167]
	v_mov_b32_e32 v4, v3
	v_cvt_pk_fp8_f32 v4, v172, v173
	v_min_f32_e32 v6, 0x40e00000, v160
	v_mov_b32_e32 v5, v3
	v_cvt_pk_fp8_f32 v4, v174, v175 op_sel:[0,0,1]
	v_med3_f32 v7, v156, s2, v200
	v_mul_f32_e32 v7, v6, v7
	v_mul_f32_e32 v6, 0xc01d265f, v6
	v_exp_f32_e32 v6, v6
	v_med3_f32 v13, v157, s2, v200
	v_cvt_pk_fp8_f32 v5, v164, v165
	v_med3_f32 v14, v158, s2, v200
	v_add_f32_e32 v6, 1.0, v6
	v_rcp_f32_e32 v6, v6
	v_med3_f32 v15, v159, s2, v200
	v_cvt_pk_fp8_f32 v5, v166, v167 op_sel:[0,0,1]
	v_med3_f32 v148, v148, s2, v200
	v_mul_f32_e32 v7, v6, v7
	v_min_f32_e32 v6, 0x40e00000, v161
	v_mul_f32_e32 v13, v6, v13
	v_mul_f32_e32 v6, 0xc01d265f, v6
	v_exp_f32_e32 v6, v6
	v_med3_f32 v149, v149, s2, v200
	v_add_f32_e32 v6, 1.0, v6
	v_rcp_f32_e32 v6, v6
	s_nop 0
	v_mul_f32_e32 v13, v6, v13
	v_min_f32_e32 v6, 0x40e00000, v162
	v_mul_f32_e32 v14, v6, v14
	v_mul_f32_e32 v6, 0xc01d265f, v6
	v_exp_f32_e32 v6, v6
	s_nop 0
	v_add_f32_e32 v6, 1.0, v6
	v_rcp_f32_e32 v6, v6
	s_nop 0
	v_mul_f32_e32 v14, v6, v14
	v_min_f32_e32 v6, 0x40e00000, v163
	v_mul_f32_e32 v15, v6, v15
	v_mul_f32_e32 v6, 0xc01d265f, v6
	v_exp_f32_e32 v6, v6
	s_nop 0
	v_add_f32_e32 v6, 1.0, v6
	v_rcp_f32_e32 v6, v6
	s_nop 0
	v_mul_f32_e32 v15, v6, v15
	v_min_f32_e32 v152, 0x40e00000, v152
	v_min_f32_e32 v153, 0x40e00000, v153
	v_min_f32_e32 v154, 0x40e00000, v154
	v_min_f32_e32 v155, 0x40e00000, v155
	v_pk_mul_f32 v[148:149], v[152:153], v[148:149]
	v_pk_mul_f32 v[150:151], v[154:155], v[150:151]
	v_pk_mul_f32 v[152:153], v[152:153], s[84:85] op_sel_hi:[1,0]
	v_pk_mul_f32 v[154:155], v[154:155], s[84:85] op_sel_hi:[1,0]
	v_exp_f32_e32 v152, v152
	v_exp_f32_e32 v153, v153
	v_exp_f32_e32 v154, v154
	v_exp_f32_e32 v155, v155
	v_pk_add_f32 v[152:153], v[152:153], 1.0 op_sel_hi:[1,0]
	v_pk_add_f32 v[154:155], v[154:155], 1.0 op_sel_hi:[1,0]
	v_rcp_f32_e32 v152, v152
	v_rcp_f32_e32 v153, v153
	v_rcp_f32_e32 v154, v154
	v_rcp_f32_e32 v155, v155
	v_pk_mul_f32 v[148:149], v[152:153], v[148:149]
	v_pk_mul_f32 v[150:151], v[154:155], v[150:151]
	v_mov_b32_e32 v6, v3
	v_cvt_pk_fp8_f32 v6, v7, v13
	v_mov_b32_e32 v7, v3
	v_cvt_pk_fp8_f32 v7, v148, v149
	v_med3_f32 v143, v143, s2, v200
	v_cvt_pk_fp8_f32 v6, v14, v15 op_sel:[0,0,1]
	v_or_b32_e32 v14, v10, v12
	v_mov_b32_e32 v15, v11
	v_cvt_pk_fp8_f32 v7, v150, v151 op_sel:[0,0,1]
	v_lshlrev_b64 v[14:15], 10, v[14:15]
	v_lshl_add_u64 v[14:15], s[10:11], 0, v[14:15]
	v_lshl_add_u64 v[14:15], v[14:15], 0, s[12:13]
	v_lshl_add_u64 v[14:15], v[14:15], 0, v[2:3]
	v_permlane16_swap_b32_e32 v4, v6
	v_permlane16_swap_b32_e32 v5, v7
	v_lshl_add_u64 v[14:15], v[14:15], 0, v[8:9]
	global_store_dwordx4 v[14:15], v[4:7], off
	v_med3_f32 v132, v132, s2, v200
	v_med3_f32 v133, v133, s2, v200
	v_med3_f32 v140, v140, s2, v200
	v_med3_f32 v141, v141, s2, v200
	v_med3_f32 v142, v142, s2, v200
	v_med3_f32 v134, v134, s2, v200
	v_med3_f32 v135, v135, s2, v200
	v_med3_f32 v118, v118, s2, v200
	v_med3_f32 v119, v119, s2, v200
	v_min_f32_e32 v144, 0x40e00000, v144
	v_min_f32_e32 v145, 0x40e00000, v145
	v_min_f32_e32 v146, 0x40e00000, v146
	v_min_f32_e32 v147, 0x40e00000, v147
	v_pk_mul_f32 v[140:141], v[144:145], v[140:141]
	v_pk_mul_f32 v[142:143], v[146:147], v[142:143]
	v_pk_mul_f32 v[144:145], v[144:145], s[84:85] op_sel_hi:[1,0]
	v_pk_mul_f32 v[146:147], v[146:147], s[84:85] op_sel_hi:[1,0]
	v_exp_f32_e32 v144, v144
	v_exp_f32_e32 v145, v145
	v_exp_f32_e32 v146, v146
	v_exp_f32_e32 v147, v147
	v_pk_add_f32 v[144:145], v[144:145], 1.0 op_sel_hi:[1,0]
	v_pk_add_f32 v[146:147], v[146:147], 1.0 op_sel_hi:[1,0]
	v_rcp_f32_e32 v144, v144
	v_rcp_f32_e32 v145, v145
	v_rcp_f32_e32 v146, v146
	v_rcp_f32_e32 v147, v147
	v_pk_mul_f32 v[140:141], v[144:145], v[140:141]
	v_pk_mul_f32 v[142:143], v[146:147], v[142:143]
	v_min_f32_e32 v136, 0x40e00000, v136
	v_min_f32_e32 v137, 0x40e00000, v137
	v_min_f32_e32 v138, 0x40e00000, v138
	v_min_f32_e32 v139, 0x40e00000, v139
	v_pk_mul_f32 v[132:133], v[136:137], v[132:133]
	v_pk_mul_f32 v[134:135], v[138:139], v[134:135]
	v_pk_mul_f32 v[136:137], v[136:137], s[84:85] op_sel_hi:[1,0]
	v_pk_mul_f32 v[138:139], v[138:139], s[84:85] op_sel_hi:[1,0]
	v_exp_f32_e32 v136, v136
	v_exp_f32_e32 v137, v137
	v_exp_f32_e32 v138, v138
	v_exp_f32_e32 v139, v139
	v_pk_add_f32 v[136:137], v[136:137], 1.0 op_sel_hi:[1,0]
	v_pk_add_f32 v[138:139], v[138:139], 1.0 op_sel_hi:[1,0]
	v_rcp_f32_e32 v136, v136
	v_rcp_f32_e32 v137, v137
	v_rcp_f32_e32 v138, v138
	v_rcp_f32_e32 v139, v139
	v_pk_mul_f32 v[132:133], v[136:137], v[132:133]
	v_pk_mul_f32 v[134:135], v[138:139], v[134:135]
	v_mov_b32_e32 v4, v3
	v_cvt_pk_fp8_f32 v4, v140, v141
	v_min_f32_e32 v6, 0x40e00000, v128
	v_mov_b32_e32 v5, v3
	v_cvt_pk_fp8_f32 v4, v142, v143 op_sel:[0,0,1]
	v_med3_f32 v7, v124, s2, v200
	v_mul_f32_e32 v7, v6, v7
	v_mul_f32_e32 v6, 0xc01d265f, v6
	v_exp_f32_e32 v6, v6
	v_med3_f32 v13, v125, s2, v200
	v_cvt_pk_fp8_f32 v5, v132, v133
	v_med3_f32 v14, v126, s2, v200
	v_add_f32_e32 v6, 1.0, v6
	v_rcp_f32_e32 v6, v6
	v_med3_f32 v15, v127, s2, v200
	v_cvt_pk_fp8_f32 v5, v134, v135 op_sel:[0,0,1]
	v_med3_f32 v116, v116, s2, v200
	v_mul_f32_e32 v7, v6, v7
	v_min_f32_e32 v6, 0x40e00000, v129
	v_mul_f32_e32 v13, v6, v13
	v_mul_f32_e32 v6, 0xc01d265f, v6
	v_exp_f32_e32 v6, v6
	v_med3_f32 v117, v117, s2, v200
	v_add_f32_e32 v6, 1.0, v6
	v_rcp_f32_e32 v6, v6
	s_nop 0
	v_mul_f32_e32 v13, v6, v13
	v_min_f32_e32 v6, 0x40e00000, v130
	v_mul_f32_e32 v14, v6, v14
	v_mul_f32_e32 v6, 0xc01d265f, v6
	v_exp_f32_e32 v6, v6
	s_nop 0
	v_add_f32_e32 v6, 1.0, v6
	v_rcp_f32_e32 v6, v6
	s_nop 0
	v_mul_f32_e32 v14, v6, v14
	v_min_f32_e32 v6, 0x40e00000, v131
	v_mul_f32_e32 v15, v6, v15
	v_mul_f32_e32 v6, 0xc01d265f, v6
	v_exp_f32_e32 v6, v6
	s_nop 0
	v_add_f32_e32 v6, 1.0, v6
	v_rcp_f32_e32 v6, v6
	s_nop 0
	v_mul_f32_e32 v15, v6, v15
	v_min_f32_e32 v120, 0x40e00000, v120
	v_min_f32_e32 v121, 0x40e00000, v121
	v_min_f32_e32 v122, 0x40e00000, v122
	v_min_f32_e32 v123, 0x40e00000, v123
	v_pk_mul_f32 v[116:117], v[120:121], v[116:117]
	v_pk_mul_f32 v[118:119], v[122:123], v[118:119]
	v_pk_mul_f32 v[120:121], v[120:121], s[84:85] op_sel_hi:[1,0]
	v_pk_mul_f32 v[122:123], v[122:123], s[84:85] op_sel_hi:[1,0]
	v_exp_f32_e32 v120, v120
	v_exp_f32_e32 v121, v121
	v_exp_f32_e32 v122, v122
	v_exp_f32_e32 v123, v123
	v_pk_add_f32 v[120:121], v[120:121], 1.0 op_sel_hi:[1,0]
	v_pk_add_f32 v[122:123], v[122:123], 1.0 op_sel_hi:[1,0]
	v_rcp_f32_e32 v120, v120
	v_rcp_f32_e32 v121, v121
	v_rcp_f32_e32 v122, v122
	v_rcp_f32_e32 v123, v123
	v_pk_mul_f32 v[116:117], v[120:121], v[116:117]
	v_pk_mul_f32 v[118:119], v[122:123], v[118:119]
	v_mov_b32_e32 v6, v3
	v_cvt_pk_fp8_f32 v6, v7, v13
	v_mov_b32_e32 v7, v3
	v_cvt_pk_fp8_f32 v7, v116, v117
	v_or_b32_e32 v13, 32, v12
	v_cvt_pk_fp8_f32 v6, v14, v15 op_sel:[0,0,1]
	v_or_b32_e32 v14, v10, v13
	v_mov_b32_e32 v15, v11
	v_cvt_pk_fp8_f32 v7, v118, v119 op_sel:[0,0,1]
	v_lshlrev_b64 v[14:15], 10, v[14:15]
	v_lshl_add_u64 v[14:15], s[10:11], 0, v[14:15]
	v_lshl_add_u64 v[14:15], v[14:15], 0, s[12:13]
	v_lshl_add_u64 v[14:15], v[14:15], 0, v[2:3]
	v_permlane16_swap_b32_e32 v4, v6
	v_permlane16_swap_b32_e32 v5, v7
	v_lshl_add_u64 v[14:15], v[14:15], 0, v[8:9]
	global_store_dwordx4 v[14:15], v[4:7], off
	v_med3_f32 v111, v111, s2, v200
	v_med3_f32 v100, v100, s2, v200
	v_med3_f32 v108, v108, s2, v200
	v_med3_f32 v109, v109, s2, v200
	v_med3_f32 v110, v110, s2, v200
	v_med3_f32 v101, v101, s2, v200
	v_med3_f32 v102, v102, s2, v200
	v_med3_f32 v103, v103, s2, v200
	v_med3_f32 v86, v86, s2, v200
	v_lshl_add_u64 v[10:11], v[10:11], 0, s[52:53]
	v_min_f32_e32 v112, 0x40e00000, v112
	v_min_f32_e32 v113, 0x40e00000, v113
	v_min_f32_e32 v114, 0x40e00000, v114
	v_min_f32_e32 v115, 0x40e00000, v115
	v_pk_mul_f32 v[108:109], v[112:113], v[108:109]
	v_pk_mul_f32 v[110:111], v[114:115], v[110:111]
	v_pk_mul_f32 v[112:113], v[112:113], s[84:85] op_sel_hi:[1,0]
	v_pk_mul_f32 v[114:115], v[114:115], s[84:85] op_sel_hi:[1,0]
	v_exp_f32_e32 v112, v112
	v_exp_f32_e32 v113, v113
	v_exp_f32_e32 v114, v114
	v_exp_f32_e32 v115, v115
	v_pk_add_f32 v[112:113], v[112:113], 1.0 op_sel_hi:[1,0]
	v_pk_add_f32 v[114:115], v[114:115], 1.0 op_sel_hi:[1,0]
	v_rcp_f32_e32 v112, v112
	v_rcp_f32_e32 v113, v113
	v_rcp_f32_e32 v114, v114
	v_rcp_f32_e32 v115, v115
	v_pk_mul_f32 v[108:109], v[112:113], v[108:109]
	v_pk_mul_f32 v[110:111], v[114:115], v[110:111]
	v_min_f32_e32 v104, 0x40e00000, v104
	v_min_f32_e32 v105, 0x40e00000, v105
	v_min_f32_e32 v106, 0x40e00000, v106
	v_min_f32_e32 v107, 0x40e00000, v107
	v_pk_mul_f32 v[100:101], v[104:105], v[100:101]
	v_pk_mul_f32 v[102:103], v[106:107], v[102:103]
	v_pk_mul_f32 v[104:105], v[104:105], s[84:85] op_sel_hi:[1,0]
	v_pk_mul_f32 v[106:107], v[106:107], s[84:85] op_sel_hi:[1,0]
	v_exp_f32_e32 v104, v104
	v_exp_f32_e32 v105, v105
	v_exp_f32_e32 v106, v106
	v_exp_f32_e32 v107, v107
	v_pk_add_f32 v[104:105], v[104:105], 1.0 op_sel_hi:[1,0]
	v_pk_add_f32 v[106:107], v[106:107], 1.0 op_sel_hi:[1,0]
	v_rcp_f32_e32 v104, v104
	v_rcp_f32_e32 v105, v105
	v_rcp_f32_e32 v106, v106
	v_rcp_f32_e32 v107, v107
	v_pk_mul_f32 v[100:101], v[104:105], v[100:101]
	v_pk_mul_f32 v[102:103], v[106:107], v[102:103]
	v_mov_b32_e32 v4, v3
	v_cvt_pk_fp8_f32 v4, v108, v109
	v_min_f32_e32 v6, 0x40e00000, v96
	v_mov_b32_e32 v5, v3
	v_cvt_pk_fp8_f32 v4, v110, v111 op_sel:[0,0,1]
	v_med3_f32 v7, v92, s2, v200
	v_mul_f32_e32 v7, v6, v7
	v_mul_f32_e32 v6, 0xc01d265f, v6
	v_exp_f32_e32 v6, v6
	v_med3_f32 v14, v93, s2, v200
	v_cvt_pk_fp8_f32 v5, v100, v101
	v_med3_f32 v15, v94, s2, v200
	v_add_f32_e32 v6, 1.0, v6
	v_rcp_f32_e32 v6, v6
	v_med3_f32 v16, v95, s2, v200
	v_cvt_pk_fp8_f32 v5, v102, v103 op_sel:[0,0,1]
	v_med3_f32 v84, v84, s2, v200
	v_mul_f32_e32 v7, v6, v7
	v_min_f32_e32 v6, 0x40e00000, v97
	v_mul_f32_e32 v14, v6, v14
	v_mul_f32_e32 v6, 0xc01d265f, v6
	v_exp_f32_e32 v6, v6
	v_med3_f32 v85, v85, s2, v200
	v_add_f32_e32 v6, 1.0, v6
	v_rcp_f32_e32 v6, v6
	s_nop 0
	v_mul_f32_e32 v14, v6, v14
	v_min_f32_e32 v6, 0x40e00000, v98
	v_mul_f32_e32 v15, v6, v15
	v_mul_f32_e32 v6, 0xc01d265f, v6
	v_exp_f32_e32 v6, v6
	s_nop 0
	v_add_f32_e32 v6, 1.0, v6
	v_rcp_f32_e32 v6, v6
	s_nop 0
	v_mul_f32_e32 v15, v6, v15
	v_min_f32_e32 v6, 0x40e00000, v99
	v_mul_f32_e32 v16, v6, v16
	v_mul_f32_e32 v6, 0xc01d265f, v6
	v_exp_f32_e32 v6, v6
	s_nop 0
	v_add_f32_e32 v6, 1.0, v6
	v_rcp_f32_e32 v6, v6
	s_nop 0
	v_mul_f32_e32 v16, v6, v16
	v_min_f32_e32 v88, 0x40e00000, v88
	v_min_f32_e32 v89, 0x40e00000, v89
	v_min_f32_e32 v90, 0x40e00000, v90
	v_min_f32_e32 v91, 0x40e00000, v91
	v_pk_mul_f32 v[84:85], v[88:89], v[84:85]
	v_pk_mul_f32 v[86:87], v[90:91], v[86:87]
	v_pk_mul_f32 v[88:89], v[88:89], s[84:85] op_sel_hi:[1,0]
	v_pk_mul_f32 v[90:91], v[90:91], s[84:85] op_sel_hi:[1,0]
	v_exp_f32_e32 v88, v88
	v_exp_f32_e32 v89, v89
	v_exp_f32_e32 v90, v90
	v_exp_f32_e32 v91, v91
	v_pk_add_f32 v[88:89], v[88:89], 1.0 op_sel_hi:[1,0]
	v_pk_add_f32 v[90:91], v[90:91], 1.0 op_sel_hi:[1,0]
	v_rcp_f32_e32 v88, v88
	v_rcp_f32_e32 v89, v89
	v_rcp_f32_e32 v90, v90
	v_rcp_f32_e32 v91, v91
	v_pk_mul_f32 v[84:85], v[88:89], v[84:85]
	v_pk_mul_f32 v[86:87], v[90:91], v[86:87]
	v_mov_b32_e32 v6, v3
	v_cvt_pk_fp8_f32 v6, v7, v14
	v_mov_b32_e32 v7, v3
	v_cvt_pk_fp8_f32 v7, v84, v85
	v_or_b32_e32 v14, v10, v12
	v_cvt_pk_fp8_f32 v6, v15, v16 op_sel:[0,0,1]
	v_mov_b32_e32 v15, v11
	v_cvt_pk_fp8_f32 v7, v86, v87 op_sel:[0,0,1]
	v_lshlrev_b64 v[14:15], 10, v[14:15]
	v_lshl_add_u64 v[14:15], s[10:11], 0, v[14:15]
	v_lshl_add_u64 v[14:15], v[14:15], 0, s[12:13]
	v_lshl_add_u64 v[14:15], v[14:15], 0, v[2:3]
	v_permlane16_swap_b32_e32 v4, v6
	v_permlane16_swap_b32_e32 v5, v7
	v_lshl_add_u64 v[14:15], v[14:15], 0, v[8:9]
	global_store_dwordx4 v[14:15], v[4:7], off
	v_med3_f32 v79, v79, s2, v200
	v_med3_f32 v68, v68, s2, v200
	v_med3_f32 v76, v76, s2, v200
	v_med3_f32 v77, v77, s2, v200
	v_med3_f32 v78, v78, s2, v200
	v_med3_f32 v69, v69, s2, v200
	v_med3_f32 v70, v70, s2, v200
	v_med3_f32 v71, v71, s2, v200
	v_med3_f32 v54, v54, s2, v200
	v_med3_f32 v55, v55, s2, v200
	v_or_b32_e32 v10, v10, v13
	v_lshlrev_b64 v[10:11], 10, v[10:11]
	v_lshl_add_u64 v[10:11], s[10:11], 0, v[10:11]
	v_lshl_add_u64 v[10:11], v[10:11], 0, s[12:13]
	v_lshl_add_u64 v[10:11], v[10:11], 0, v[2:3]
	v_lshl_add_u64 v[8:9], v[10:11], 0, v[8:9]
	v_min_f32_e32 v80, 0x40e00000, v80
	v_min_f32_e32 v81, 0x40e00000, v81
	v_min_f32_e32 v82, 0x40e00000, v82
	v_min_f32_e32 v83, 0x40e00000, v83
	v_pk_mul_f32 v[76:77], v[80:81], v[76:77]
	v_pk_mul_f32 v[78:79], v[82:83], v[78:79]
	v_pk_mul_f32 v[80:81], v[80:81], s[84:85] op_sel_hi:[1,0]
	v_pk_mul_f32 v[82:83], v[82:83], s[84:85] op_sel_hi:[1,0]
	v_exp_f32_e32 v80, v80
	v_exp_f32_e32 v81, v81
	v_exp_f32_e32 v82, v82
	v_exp_f32_e32 v83, v83
	v_pk_add_f32 v[80:81], v[80:81], 1.0 op_sel_hi:[1,0]
	v_pk_add_f32 v[82:83], v[82:83], 1.0 op_sel_hi:[1,0]
	v_rcp_f32_e32 v80, v80
	v_rcp_f32_e32 v81, v81
	v_rcp_f32_e32 v82, v82
	v_rcp_f32_e32 v83, v83
	v_pk_mul_f32 v[76:77], v[80:81], v[76:77]
	v_pk_mul_f32 v[78:79], v[82:83], v[78:79]
	v_min_f32_e32 v72, 0x40e00000, v72
	v_min_f32_e32 v73, 0x40e00000, v73
	v_min_f32_e32 v74, 0x40e00000, v74
	v_min_f32_e32 v75, 0x40e00000, v75
	v_pk_mul_f32 v[68:69], v[72:73], v[68:69]
	v_pk_mul_f32 v[70:71], v[74:75], v[70:71]
	v_pk_mul_f32 v[72:73], v[72:73], s[84:85] op_sel_hi:[1,0]
	v_pk_mul_f32 v[74:75], v[74:75], s[84:85] op_sel_hi:[1,0]
	v_exp_f32_e32 v72, v72
	v_exp_f32_e32 v73, v73
	v_exp_f32_e32 v74, v74
	v_exp_f32_e32 v75, v75
	v_pk_add_f32 v[72:73], v[72:73], 1.0 op_sel_hi:[1,0]
	v_pk_add_f32 v[74:75], v[74:75], 1.0 op_sel_hi:[1,0]
	v_rcp_f32_e32 v72, v72
	v_rcp_f32_e32 v73, v73
	v_rcp_f32_e32 v74, v74
	v_rcp_f32_e32 v75, v75
	v_pk_mul_f32 v[68:69], v[72:73], v[68:69]
	v_pk_mul_f32 v[70:71], v[74:75], v[70:71]
	v_mov_b32_e32 v4, v3
	v_cvt_pk_fp8_f32 v4, v76, v77
	v_min_f32_e32 v6, 0x40e00000, v64
	v_mov_b32_e32 v5, v3
	v_cvt_pk_fp8_f32 v4, v78, v79 op_sel:[0,0,1]
	v_med3_f32 v7, v60, s2, v200
	v_mul_f32_e32 v7, v6, v7
	v_mul_f32_e32 v6, 0xc01d265f, v6
	v_exp_f32_e32 v6, v6
	v_med3_f32 v12, v61, s2, v200
	v_cvt_pk_fp8_f32 v5, v68, v69
	v_med3_f32 v14, v62, s2, v200
	v_add_f32_e32 v6, 1.0, v6
	v_rcp_f32_e32 v6, v6
	v_med3_f32 v15, v63, s2, v200
	v_cvt_pk_fp8_f32 v5, v70, v71 op_sel:[0,0,1]
	v_med3_f32 v52, v52, s2, v200
	v_mul_f32_e32 v7, v6, v7
	v_min_f32_e32 v6, 0x40e00000, v65
	v_mul_f32_e32 v12, v6, v12
	v_mul_f32_e32 v6, 0xc01d265f, v6
	v_exp_f32_e32 v6, v6
	v_med3_f32 v53, v53, s2, v200
	s_mov_b64 s[2:3], -1
	v_add_f32_e32 v6, 1.0, v6
	v_rcp_f32_e32 v6, v6
	s_nop 0
	v_mul_f32_e32 v12, v6, v12
	v_min_f32_e32 v6, 0x40e00000, v66
	v_mul_f32_e32 v14, v6, v14
	v_mul_f32_e32 v6, 0xc01d265f, v6
	v_exp_f32_e32 v6, v6
	s_nop 0
	v_add_f32_e32 v6, 1.0, v6
	v_rcp_f32_e32 v6, v6
	s_nop 0
	v_mul_f32_e32 v14, v6, v14
	v_min_f32_e32 v6, 0x40e00000, v67
	v_mul_f32_e32 v15, v6, v15
	v_mul_f32_e32 v6, 0xc01d265f, v6
	v_exp_f32_e32 v6, v6
	s_nop 0
	v_add_f32_e32 v6, 1.0, v6
	v_rcp_f32_e32 v6, v6
	s_nop 0
	v_mul_f32_e32 v15, v6, v15
	v_min_f32_e32 v56, 0x40e00000, v56
	v_min_f32_e32 v57, 0x40e00000, v57
	v_min_f32_e32 v58, 0x40e00000, v58
	v_min_f32_e32 v59, 0x40e00000, v59
	v_pk_mul_f32 v[52:53], v[56:57], v[52:53]
	v_pk_mul_f32 v[54:55], v[58:59], v[54:55]
	v_pk_mul_f32 v[56:57], v[56:57], s[84:85] op_sel_hi:[1,0]
	v_pk_mul_f32 v[58:59], v[58:59], s[84:85] op_sel_hi:[1,0]
	v_exp_f32_e32 v56, v56
	v_exp_f32_e32 v57, v57
	v_exp_f32_e32 v58, v58
	v_exp_f32_e32 v59, v59
	v_pk_add_f32 v[56:57], v[56:57], 1.0 op_sel_hi:[1,0]
	v_pk_add_f32 v[58:59], v[58:59], 1.0 op_sel_hi:[1,0]
	v_rcp_f32_e32 v56, v56
	v_rcp_f32_e32 v57, v57
	v_rcp_f32_e32 v58, v58
	v_rcp_f32_e32 v59, v59
	v_pk_mul_f32 v[52:53], v[56:57], v[52:53]
	v_pk_mul_f32 v[54:55], v[58:59], v[54:55]
	v_mov_b32_e32 v6, v3
	v_cvt_pk_fp8_f32 v6, v7, v12
	v_mov_b32_e32 v7, v3
	v_cvt_pk_fp8_f32 v7, v52, v53
	v_cvt_pk_fp8_f32 v6, v14, v15 op_sel:[0,0,1]
	v_cvt_pk_fp8_f32 v7, v54, v55 op_sel:[0,0,1]
	s_nop 0
	v_permlane16_swap_b32_e32 v4, v6
	v_permlane16_swap_b32_e32 v5, v7
	global_store_dwordx4 v[8:9], v[4:7], off
	s_cbranch_vccnz .LBB0_1269
	s_and_saveexec_b64 s[2:3], s[36:37]
	s_xor_b64 s[2:3], exec, s[2:3]
	s_cbranch_execz .LBB0_1268
	s_barrier
